# attn: key-tile rotation (2qb+9head)&31
# speedup vs baseline: 1.0291x; 1.0291x over previous
.Lp_top:
	s_lshl_b32 s6, s21, 20
	s_add_u32 s4, s4, s6
	s_addc_u32 s5, s5, 0
	v_lshlrev_b32_e32 v54, 4, v0
	v_mov_b32_e32 v55, v63
	s_lshl_b32 s3, s3, 1
	s_mul_i32 s20, s21, 9
	v_lshl_add_u64 v[4:5], s[4:5], 0, v[54:55]
	s_mov_b64 s[4:5], 0x1000000
	s_add_i32 s20, s20, s3
	v_lshl_add_u64 v[170:171], v[4:5], 0, s[4:5]
	s_and_b32 s22, s20, 31
	s_lshl_b32 s4, s20, 12
	s_lshl_b32 s12, s22, 13
	s_add_i32 s5, s4, 0x1000
	v_lshl_add_u64 v[58:59], v[170:171], 0, s[12:13]
	s_mov_b32 s3, 0x80000
	s_and_b32 s5, s5, 0x1f000
	v_add_co_u32_e32 v16, vcc, s3, v58
	s_lshl_b32 s12, s5, 1
	s_nop 0
	v_addc_co_u32_e32 v17, vcc, 0, v59, vcc
	v_lshl_add_u64 v[56:57], v[170:171], 0, s[12:13]
	global_load_dwordx4 v[4:7], v[58:59], off
	global_load_dwordx4 v[8:11], v[56:57], off
	global_load_dwordx4 v[12:15], v[16:17], off
	v_add_co_u32_e32 v16, vcc, s3, v56
	v_lshrrev_b32_e32 v184, 8, v0
	s_nop 0
	v_addc_co_u32_e32 v17, vcc, 0, v57, vcc
	global_load_dwordx4 v[16:19], v[16:17], off
	v_and_b32_e32 v20, 19, v0
	v_lshlrev_b32_e32 v21, 1, v0
	v_and_b32_e32 v2, 4, v2
	v_and_or_b32 v20, v21, 8, v20
	v_lshlrev_b32_e32 v101, 5, v184
	s_addk_i32 s4, 0x2000
	v_or3_b32 v2, v20, v2, v101
	s_and_b32 s4, s4, 0x1f000
	v_mul_u32_u24_e32 v2, 0x48, v2
	s_lshl_b32 s12, s4, 1
	v_lshlrev_b32_e32 v3, 3, v0
	v_lshlrev_b32_e32 v100, 1, v99
	v_lshlrev_b32_e32 v2, 1, v2
	v_lshl_add_u64 v[60:61], v[170:171], 0, s[12:13]
	v_and_b32_e32 v3, 56, v3
	v_add3_u32 v186, 0, v2, v100
	v_add_co_u32_e32 v2, vcc, s3, v60
	v_lshlrev_b32_e32 v68, 1, v3
	s_nop 0
	v_addc_co_u32_e32 v3, vcc, 0, v61, vcc
	global_load_dwordx4 v[162:165], v[60:61], off
	global_load_dwordx4 v[166:169], v[2:3], off
	v_lshrrev_b32_e32 v82, 3, v0
	v_mul_u32_u24_e32 v22, 0x48, v82
	v_lshlrev_b32_e32 v21, 1, v22
	v_add3_u32 v185, 0, v21, v68
	s_mov_b64 s[24:25], 0x80000
	s_add_i32 s17, s20, 3
	s_add_i32 s18, s20, 4
	v_mov_b32_e32 v62, v63
	v_lshrrev_b32_e32 v55, 6, v0
	v_mov_b32_e32 v83, 0
	v_mov_b32_e32 v84, 0
	v_lshl_add_u64 v[70:71], v[58:59], 0, s[24:25]
	v_lshl_add_u64 v[66:67], v[56:57], 0, s[24:25]
	v_lshl_add_u64 v[64:65], v[60:61], 0, s[24:25]
	s_waitcnt vmcnt(5)
	ds_write_b128 v185, v[4:7]
	s_waitcnt vmcnt(3)
	ds_write_b128 v185, v[12:15] offset:9216
	ds_write_b128 v185, v[8:11] offset:18432
	s_waitcnt vmcnt(2)
	ds_write_b128 v185, v[16:19] offset:27648
	s_waitcnt lgkmcnt(0)
	s_barrier
	ds_read_b128 v[2:5], v186
	ds_read_b128 v[38:41], v186 offset:32
	s_waitcnt lgkmcnt(1)
	v_mfma_f32_32x32x16_f16 v[2:17], v[2:5], v[114:117], 0
	ds_read_b128 v[18:21], v186 offset:9216
	ds_read_b128 v[46:49], v186 offset:9248
	s_waitcnt lgkmcnt(1)
	v_mfma_f32_32x32x16_f16 v[18:33], v[18:21], v[130:133], 0
	v_mfma_f32_32x32x16_f16 v[2:17], v[38:41], v[118:121], v[2:17]
	s_waitcnt lgkmcnt(0)
	v_mfma_f32_32x32x16_f16 v[18:33], v[46:49], v[134:137], v[18:33]
	ds_read_b128 v[38:41], v186 offset:64
	ds_read_b128 v[46:49], v186 offset:96
	s_waitcnt lgkmcnt(1)
	v_mfma_f32_32x32x16_f16 v[2:17], v[38:41], v[122:125], v[2:17]
	ds_read_b128 v[38:41], v186 offset:9280
	ds_read_b128 v[50:53], v186 offset:9312
	s_load_dwordx4 s[4:7], s[0:1], 0x38
	s_load_dwordx2 s[14:15], s[0:1], 0x8
	s_mov_b32 s0, -2
	s_mov_b32 s1, 0x3f800000
	s_waitcnt lgkmcnt(0)
	s_barrier
	v_mfma_f32_32x32x16_f16 v[18:33], v[38:41], v[138:141], v[18:33]
	v_mfma_f32_32x32x16_f16 v[2:17], v[46:49], v[126:129], v[2:17]
	v_mfma_f32_32x32x16_f16 v[18:33], v[50:53], v[142:145], v[18:33]
	s_lshl_b32 s12, s17, 13
	s_and_b32 s12, s12, 0x3e000
	s_add_u32 s28, s12, s3
	s_mov_b32 s29, 0
	v_lshl_add_u64 v[176:177], v[170:171], 0, s[12:13]
	global_load_dwordx4 v[50:53], v[176:177], off
	v_lshl_add_u64 v[176:177], v[170:171], 0, s[28:29]
	global_load_dwordx4 v[94:97], v[176:177], off
	s_nop 7
	s_cmp_eq_u32 s37, 1
	s_cbranch_scc0 .Lf_A
	v_mov_b32_e32 v83, 0xf149f2ca
	v_mov_b32_e32 v84, 0xf149f2ca
	s_branch .Ls_A

.Ll1_cont:
	ds_bpermute_b32 v2, v69, v84
	ds_bpermute_b32 v5, v69, v83
	v_max_f32_e32 v4, v84, v84
	v_max_f32_e32 v7, v83, v83
	ds_bpermute_b32 v3, v69, v63
	s_waitcnt lgkmcnt(2)
	v_max_f32_e32 v6, v2, v2
	v_max_f32_e32 v4, v4, v6
	v_sub_f32_e32 v6, v84, v4
	v_exp_f32_e32 v9, v6
	s_waitcnt lgkmcnt(1)
	v_max_f32_e32 v6, v5, v5
	v_sub_f32_e32 v2, v2, v4
	v_max_f32_e32 v6, v7, v6
	v_exp_f32_e32 v11, v2
	ds_bpermute_b32 v2, v69, v62
	v_sub_f32_e32 v5, v5, v6
	v_sub_f32_e32 v7, v83, v6
	v_exp_f32_e32 v10, v5
	v_exp_f32_e32 v8, v7
	v_cmp_gt_u32_e32 vcc, 32, v98
	s_waitcnt lgkmcnt(0)
	v_pk_mul_f32 v[2:3], v[10:11], v[2:3]
	s_nop 0
	v_pk_fma_f32 v[8:9], v[62:63], v[8:9], v[2:3]
	v_lshlrev_b32_e32 v2, 7, v184
	v_or3_b32 v10, v183, v2, v1
	s_and_saveexec_b64 s[0:1], vcc
	v_lshl_add_u32 v2, v10, 4, 0
	v_add_u32_e32 v2, 0x21000, v2
	v_mov_b32_e32 v5, v9
	v_mov_b32_e32 v7, v8
	ds_write_b128 v2, v[4:7]
	s_or_b64 exec, exec, s[0:1]
	s_lshl_b32 s12, s21, 7
	s_mov_b32 s3, 0
	v_or_b32_e32 v2, s12, v82
	s_lshl_b32 s13, s21, 11
	s_add_i32 s23, 0, 0x12000
	v_lshlrev_b32_e32 v2, 12, v2
	v_mov_b32_e32 v3, 0
	s_add_i32 s13, s13, s16
	s_lshl_b64 s[0:1], s[2:3], 13
	v_lshl_add_u64 v[12:13], s[14:15], 0, v[2:3]
	v_mov_b32_e32 v69, v3
	s_add_u32 s0, s10, s0
	v_lshl_add_u64 v[172:173], v[12:13], 0, v[68:69]
	s_addc_u32 s1, s11, s1
	s_lshl_b32 s10, s22, 7
	s_mov_b32 s11, s3
	s_waitcnt vmcnt(1)
	v_lshl_add_u64 v[36:37], v[172:173], 0, s[10:11]
	s_mov_b32 s10, 0x40000
	v_add_co_u32_e32 v38, vcc, s10, v36
	s_waitcnt lgkmcnt(0)
	s_barrier
	global_load_dwordx4 v[12:15], v[58:59], off
	global_load_dwordx4 v[16:19], v[70:71], off
	v_addc_co_u32_e32 v39, vcc, 0, v37, vcc
	global_load_dwordx4 v[20:23], v[56:57], off
	global_load_dwordx4 v[24:27], v[66:67], off
	global_load_dwordx4 v[28:31], v[36:37], off
	global_load_dwordx4 v[32:35], v[38:39], off
	v_add_f32_e32 v2, v78, v80
	s_movk_i32 s11, 0x1200
	v_add_f32_e32 v5, v79, v81
	s_mov_b32 s14, 0x3fb8aa3b
	v_lshlrev_b32_e32 v10, 4, v10
	v_mov_b32_e32 v36, s23
	v_mul_f32_e32 v37, 0x3fb8aa3b, v2
	v_mul_f32_e32 v38, 0x3fb8aa3b, v5
	v_xor_b32_e32 v10, 0x800, v10
	v_mad_u32_u24 v40, v55, s11, v36
	v_fma_f32 v36, v2, s14, -v37
	v_rndne_f32_e32 v39, v37
	v_fma_f32 v41, v5, s14, -v38
	s_waitcnt vmcnt(6)
	v_rndne_f32_e32 v42, v38
	v_add_u32_e32 v10, 0, v10
	v_fmac_f32_e32 v36, 0x32a5705f, v2
	v_sub_f32_e32 v37, v37, v39
	v_fmac_f32_e32 v41, 0x32a5705f, v5
	v_sub_f32_e32 v38, v38, v42
	v_add_u32_e32 v10, 0x21000, v10
	v_add_f32_e32 v44, v37, v36
	global_load_dwordx4 v[146:149], v[60:61], off
	global_load_dwordx4 v[150:153], v[64:65], off
	v_cvt_i32_f32_e32 v43, v39
	v_add_f32_e32 v41, v38, v41
	ds_read_b128 v[36:39], v10
	v_exp_f32_e32 v10, v44
	v_cvt_i32_f32_e32 v42, v42
	v_exp_f32_e32 v41, v41
	s_mov_b32 s21, 0xc2ce8ed0
	s_lshl_b32 s11, s20, 6
	s_add_i32 s14, s11, 64
	v_ldexp_f32 v10, v10, v43
	v_cmp_ngt_f32_e32 vcc, s21, v2
	s_mov_b32 s22, 0x42b17218
	s_and_b32 s14, s14, 0x7c0
	v_ldexp_f32 v41, v41, v42
	v_cndmask_b32_e32 v10, 0, v10, vcc
	v_cmp_ngt_f32_e32 vcc, s21, v5
	v_mov_b32_e32 v7, 0x7f800000
	v_max_f32_e32 v11, v4, v4
	s_mov_b32 s15, s3
	s_lshl_b32 s14, s14, 1
	s_waitcnt lgkmcnt(0)
	v_max_f32_e32 v42, v36, v36
	v_cndmask_b32_e32 v41, 0, v41, vcc
	v_cmp_nlt_f32_e32 vcc, s22, v2
	v_max_f32_e32 v187, v11, v42
	v_mov_b32_e32 v55, v3
	v_cndmask_b32_e32 v2, v7, v10, vcc
	v_cmp_nlt_f32_e32 vcc, s22, v5
	v_lshl_add_u64 v[10:11], v[172:173], 0, s[14:15]
	v_lshl_add_u64 v[178:179], s[0:1], 0, v[54:55]
	v_cndmask_b32_e32 v5, v7, v41, vcc
	v_sub_f32_e32 v2, v2, v5
	v_add_f32_e32 v41, 0x3e4ccccd, v2
	v_sub_f32_e32 v2, v4, v187
	v_max_f32_e32 v4, v6, v6
	s_and_b32 s1, s2, 7
	s_mulk_i32 s1, 0x480
	s_mulk_i32 s19, 0x240
	s_add_i32 s0, s20, 2
	s_waitcnt vmcnt(7)
	ds_write_b128 v185, v[12:15]
	s_waitcnt vmcnt(6)
	ds_write_b128 v185, v[16:19] offset:9216
	s_waitcnt vmcnt(5)
	ds_write_b128 v185, v[20:23] offset:18432
	s_waitcnt vmcnt(4)
	ds_write_b128 v185, v[24:27] offset:27648
	s_waitcnt vmcnt(3)
	ds_write_b128 v185, v[28:31] offset:36864
	s_waitcnt vmcnt(2)
	ds_write_b128 v185, v[32:35] offset:46080
	v_add_co_u32_e32 v12, vcc, s10, v10
	v_exp_f32_e32 v23, v2
	s_nop 0
	v_addc_co_u32_e32 v13, vcc, 0, v11, vcc
	global_load_dwordx4 v[154:157], v[10:11], off
	global_load_dwordx4 v[158:161], v[12:13], off
	s_waitcnt lgkmcnt(0)
	s_barrier
	ds_read_b128 v[10:13], v186
	v_sub_f32_e32 v2, v36, v187
	v_exp_f32_e32 v25, v2
	v_max_f32_e32 v2, v38, v38
	v_max_f32_e32 v188, v4, v2
	v_sub_f32_e32 v2, v6, v188
	v_exp_f32_e32 v22, v2
	v_sub_f32_e32 v2, v38, v188
	v_exp_f32_e32 v24, v2
	ds_read_b128 v[14:17], v186 offset:9216
	ds_read_b128 v[18:21], v186 offset:32
	s_waitcnt lgkmcnt(2)
	v_mfma_f32_32x32x16_f16 v[66:81], v[10:13], v[114:117], 0
	v_mov_b32_e32 v36, v39
	v_mul_f32_e64 v10, v36, v24
	v_mul_f32_e64 v11, v37, v25
	ds_read_b128 v[4:7], v186 offset:9248
	s_add_i32 s1, s1, s19
	s_mov_b32 s14, 0x30000
	s_mov_b32 s15, 0x80000
	s_mov_b32 s19, 0
	s_waitcnt lgkmcnt(2)
	v_mfma_f32_32x32x16_f16 v[82:97], v[14:17], v[130:133], 0
	v_fma_f32 v16, v8, v22, v10
	v_fma_f32 v17, v9, v23, v11
	v_log_f32_e32 v238, v17
	s_nop 0
	v_add_f32_e32 v187, v187, v238
	v_sub_f32_e32 v240, 0, v187
	v_sub_f32_e32 v241, 0, v187
	v_sub_f32_e32 v242, 0, v187
	v_sub_f32_e32 v243, 0, v187
	v_sub_f32_e32 v244, 0, v187
	v_sub_f32_e32 v245, 0, v187
	v_sub_f32_e32 v246, 0, v187
	v_sub_f32_e32 v247, 0, v187
	v_sub_f32_e32 v248, 0, v187
	v_sub_f32_e32 v249, 0, v187
	v_sub_f32_e32 v250, 0, v187
	v_sub_f32_e32 v251, 0, v187
	v_sub_f32_e32 v252, 0, v187
	v_sub_f32_e32 v253, 0, v187
	v_sub_f32_e32 v254, 0, v187
	v_sub_f32_e32 v255, 0, v187
	v_lshrrev_b32_e32 v22, 3, v98
	v_or3_b32 v2, s13, v183, v22
	v_lshlrev_b64 v[8:9], 13, v[2:3]
	v_lshl_add_u64 v[8:9], s[4:5], 0, v[8:9]
	v_lshlrev_b32_e32 v2, 2, v101
	v_lshl_add_u64 v[8:9], v[8:9], 0, v[2:3]
	v_and_b32_e32 v2, 0x70, v54
	v_lshl_add_u64 v[174:175], v[8:9], 0, v[2:3]
	ds_read_b128 v[8:11], v186 offset:64
	s_waitcnt lgkmcnt(2)
	v_mfma_f32_32x32x16_f16 v[66:81], v[18:21], v[118:121], v[66:81]
	v_div_scale_f32 v18, s[4:5], v16, v16, -v41
	v_rcp_f32_e32 v19, v18
	v_div_scale_f32 v20, vcc, -v41, v16, -v41
	s_mov_b32 s13, 0x20000
	v_mov_b32_e32 v24, v3
	s_waitcnt lgkmcnt(1)
	v_mfma_f32_32x32x16_f16 v[82:97], v[4:7], v[134:137], v[82:97]
	v_fma_f32 v4, -v18, v19, 1.0
	v_fmac_f32_e32 v19, v4, v19
	v_mul_f32_e32 v21, v20, v19
	ds_read_b128 v[4:7], v186 offset:9280
	ds_read_b128 v[12:15], v186 offset:96
	v_mov_b32_e32 v25, v3
	v_mov_b32_e32 v26, v3
	v_mov_b32_e32 v27, v3
	s_waitcnt lgkmcnt(2)
	v_mfma_f32_32x32x16_f16 v[66:81], v[8:11], v[122:125], v[66:81]
	v_fma_f32 v8, -v18, v21, v20
	v_fmac_f32_e32 v21, v8, v19
	v_fma_f32 v18, -v18, v21, v20
	v_div_scale_f32 v20, s[4:5], v17, v17, 1.0
	v_rcp_f32_e32 v23, v20
	ds_read_b128 v[8:11], v186 offset:9312
	s_waitcnt lgkmcnt(2)
	v_mfma_f32_32x32x16_f16 v[82:97], v[4:7], v[138:141], v[82:97]
	v_div_fmas_f32 v4, v18, v19, v21
	v_div_fixup_f32 v176, v4, v16, -v41
	v_fma_f32 v4, -v20, v23, 1.0
	v_fmac_f32_e32 v23, v4, v23
	v_div_scale_f32 v4, vcc, 1.0, v17, 1.0
	v_mul_f32_e32 v5, v4, v23
	v_fma_f32 v6, -v20, v5, v4
	v_fmac_f32_e32 v5, v6, v23
	s_waitcnt lgkmcnt(1)
	v_mfma_f32_32x32x16_f16 v[66:81], v[12:15], v[126:129], v[66:81]
	v_fma_f32 v4, -v20, v5, v4
	v_div_fmas_f32 v4, v4, v23, v5
	v_div_fixup_f32 v177, v4, v17, 1.0
	v_mul_u32_u24_e32 v4, 0x90, v22
	v_add3_u32 v189, v40, v4, v2
	v_mul_u32_u24_e32 v2, 0x90, v1
	v_lshlrev_b32_e32 v4, 2, v99
	s_waitcnt lgkmcnt(0)
	v_mfma_f32_32x32x16_f16 v[82:97], v[8:11], v[142:145], v[82:97]
	v_add3_u32 v190, v40, v2, v4
	v_mul_u32_u24_e32 v2, 0x48, v1
	v_lshl_add_u32 v2, v2, 1, 0
	v_lshlrev_b32_e32 v4, 1, v101
	v_add3_u32 v191, v2, v4, v100
	s_mov_b32 s4, 0x3f800000
	s_mov_b32 s5, 0x10000
	v_mov_b32_e32 v2, v3
	v_mov_b32_e32 v4, v3
	v_mov_b32_e32 v5, v3
	v_mov_b32_e32 v6, v3
	v_mov_b32_e32 v7, v3
	v_mov_b32_e32 v8, v3
	v_mov_b32_e32 v9, v3
	v_mov_b32_e32 v10, v3
	v_mov_b32_e32 v11, v3
	v_mov_b32_e32 v12, v3
	v_mov_b32_e32 v13, v3
	v_mov_b32_e32 v14, v3
	v_mov_b32_e32 v15, v3
	v_mov_b32_e32 v16, v3
	v_mov_b32_e32 v17, v3
	v_mov_b32_e32 v18, v3
	v_mov_b32_e32 v19, v3
	v_mov_b32_e32 v20, v3
	v_mov_b32_e32 v21, v3
	v_mov_b32_e32 v22, v3
	v_mov_b32_e32 v23, v3
	v_mov_b32_e32 v28, v3
	v_mov_b32_e32 v29, v3
	v_mov_b32_e32 v30, v3
	v_mov_b32_e32 v31, v3
	v_mov_b32_e32 v32, v3
	v_mov_b32_e32 v33, v3
	v_mov_b32_e32 v34, v3
	v_mov_b32_e32 v35, v3
	v_mov_b32_e32 v36, v3
	v_mov_b32_e32 v37, v3
	v_mov_b32_e32 v38, v3
	v_mov_b32_e32 v39, v3
	v_mov_b32_e32 v40, v3
	v_mov_b32_e32 v41, v3
	v_mov_b32_e32 v42, v3
	v_mov_b32_e32 v43, v3
	v_mov_b32_e32 v44, v3
	v_mov_b32_e32 v45, v3
	v_mov_b32_e32 v46, v3
	v_mov_b32_e32 v47, v3
	v_mov_b32_e32 v48, v3
	v_mov_b32_e32 v49, v3
	v_mov_b32_e32 v50, v3
	v_mov_b32_e32 v51, v3
	v_mov_b32_e32 v52, v3
	v_mov_b32_e32 v53, v3
	v_mov_b32_e32 v54, v3
	v_mov_b32_e32 v56, v3
	v_mov_b32_e32 v57, v3
	v_mov_b32_e32 v58, v3
	v_mov_b32_e32 v59, v3
	v_mov_b32_e32 v60, v3
	v_mov_b32_e32 v61, v3
	v_mov_b32_e32 v62, v3
	v_mov_b32_e32 v63, v3
	v_mov_b32_e32 v64, v3
	v_mov_b32_e32 v65, v3
	v_add_u32_e32 v192, 0xd800, v191
	v_sub_f32_e32 v66, v66, v187
	v_sub_f32_e32 v67, v67, v187
	v_sub_f32_e32 v68, v68, v187
	v_sub_f32_e32 v69, v69, v187
	v_sub_f32_e32 v70, v70, v187
	v_sub_f32_e32 v71, v71, v187
	v_sub_f32_e32 v72, v72, v187
	v_sub_f32_e32 v73, v73, v187
	v_sub_f32_e32 v74, v74, v187
	v_sub_f32_e32 v75, v75, v187
	v_sub_f32_e32 v76, v76, v187
	v_sub_f32_e32 v77, v77, v187
	v_sub_f32_e32 v78, v78, v187
	v_sub_f32_e32 v79, v79, v187
	v_sub_f32_e32 v80, v80, v187
	v_sub_f32_e32 v81, v81, v187
	s_mov_b32 s27, 0x42c80000
	v_cmp_gt_f32_e64 vcc, |v188|, s27
	s_cbranch_vccnz .Ll2_gen
	v_sub_f32_e32 v238, 0, v188
	v_exp_f32_e32 v238, v238
	s_nop 0
	v_mul_f32_e32 v176, v176, v238
	s_barrier
	s_branch .Ll2f_top
